# v87 + fp8 rope epilogue: exact in-order vmcnt counts (6/8/8/8/8/8/4) so the two-ahead rope-table prefetch is really two groups deep
# baseline (speedup 1.0000x reference)
.LBB0_3488:
	v_pk_mul_f32 v[74:75], s[56:57], v[74:75] op_sel_hi:[0,1]
	v_pk_mul_f32 v[72:73], s[56:57], v[72:73] op_sel_hi:[0,1]
	v_pk_mul_f32 v[76:77], s[56:57], v[76:77] op_sel_hi:[0,1]
	v_cvt_pk_bf16_f32 v90, v74, v75
	v_cvt_pk_bf16_f32 v91, v72, v73
	v_pk_mul_f32 v[72:73], s[56:57], v[94:95] op_sel_hi:[0,1]
	v_pk_mul_f32 v[74:75], s[56:57], v[84:85] op_sel_hi:[0,1]
	s_and_b64 s[6:7], s[6:7], exec
	v_pk_mul_f32 v[78:79], s[56:57], v[78:79] op_sel_hi:[0,1]
	v_cvt_pk_bf16_f32 v89, v76, v77
	v_cvt_pk_bf16_f32 v72, v72, v73
	v_cvt_pk_bf16_f32 v73, v74, v75
	v_pk_mul_f32 v[74:75], s[56:57], v[82:83] op_sel_hi:[0,1]
	v_pk_mul_f32 v[76:77], s[56:57], v[80:81] op_sel_hi:[0,1]
	s_cselect_b32 s0, 64, 32
	v_cvt_pk_bf16_f32 v88, v78, v79
	v_cvt_pk_bf16_f32 v74, v74, v75
	v_cvt_pk_bf16_f32 v75, v76, v77
	v_lshl_add_u64 v[76:77], v[86:87], 1, s[54:55]
	s_lshl_b32 s92, s0, 1
	global_store_dwordx4 v[76:77], v[88:91], off
	v_lshl_add_u64 v[76:77], v[76:77], 0, s[92:93]
	global_store_dwordx4 v[76:77], v[72:75], off
	s_and_b64 vcc, exec, s[4:5]
	s_nop 0
	v_or_b32_e32 v72, 16, v18
	v_ashrrev_i32_e32 v73, 31, v72
	s_cbranch_vccnz .LBB0_3490
	v_lshlrev_b64 v[74:75], s64, v[72:73]
	v_lshl_add_u64 v[74:75], v[74:75], 3, v[68:69]
	v_mov_b32_e32 v94, v181
	v_mov_b32_e32 v95, v149
	s_waitcnt vmcnt(6)
	v_mov_b64_e32 v[96:97], v[106:107]
	v_mov_b64_e32 v[98:99], v[108:109]
	v_mov_b64_e32 v[84:85], v[110:111]
	v_mov_b64_e32 v[86:87], v[112:113]
	v_mov_b64_e32 v[80:81], v[114:115]
	v_mov_b64_e32 v[82:83], v[116:117]
	v_mov_b64_e32 v[76:77], v[118:119]
	v_mov_b64_e32 v[78:79], v[120:121]
	v_pk_mul_f32 v[94:95], v[94:95], v[98:99]
	v_mul_f32_e32 v100, v180, v96
	v_mul_f32_e32 v102, v148, v97
	v_mov_b32_e32 v75, v78
	v_mov_b32_e32 v78, v77
	v_mov_b32_e32 v74, v76
	v_pk_mul_f32 v[88:89], v[150:151], v[78:79]
	v_pk_mul_f32 v[76:77], v[182:183], v[78:79]
	v_mov_b32_e32 v79, v82
	v_mov_b32_e32 v82, v81
	v_mov_b32_e32 v78, v80
	v_pk_mul_f32 v[90:91], v[152:153], v[82:83]
	v_pk_mul_f32 v[80:81], v[184:185], v[82:83]
	v_mov_b32_e32 v83, v86
	v_mov_b32_e32 v86, v85
	v_mov_b32_e32 v82, v84
	v_pk_mul_f32 v[84:85], v[146:147], v[86:87]
	v_mov_b32_e32 v101, v94
	v_mov_b32_e32 v103, v95
	v_pk_fma_f32 v[94:95], v[182:183], v[74:75], v[88:89] neg_lo:[0,0,1] neg_hi:[0,0,1]
	v_pk_fma_f32 v[88:89], v[178:179], v[82:83], v[84:85] neg_lo:[0,0,1] neg_hi:[0,0,1]
	v_pk_add_f32 v[84:85], v[100:101], v[102:103] neg_lo:[0,1] neg_hi:[0,1]
	v_mov_b32_e32 v100, v149
	v_mov_b32_e32 v101, v181
	v_pk_mul_f32 v[98:99], v[100:101], v[98:99]
	v_pk_mul_f32 v[86:87], v[178:179], v[86:87]
	v_mul_f32_e32 v92, v148, v96
	v_mul_f32_e32 v96, v180, v97
	v_mov_b32_e32 v93, v98
	v_mov_b32_e32 v97, v99
	v_pk_fma_f32 v[90:91], v[184:185], v[78:79], v[90:91] neg_lo:[0,0,1] neg_hi:[0,0,1]
	v_pk_fma_f32 v[98:99], v[150:151], v[74:75], v[76:77]
	v_pk_fma_f32 v[78:79], v[152:153], v[78:79], v[80:81]
	v_pk_fma_f32 v[76:77], v[146:147], v[82:83], v[86:87]
	v_pk_add_f32 v[74:75], v[92:93], v[96:97]
	v_add_u32_e32 v128, 0x30, v18
	v_ashrrev_i32_e32 v129, 31, v128
	v_lshlrev_b64 v[128:129], s64, v[128:129]
	v_lshl_add_u64 v[128:129], v[128:129], 3, v[68:69]
	global_load_dwordx4 v[146:149], v[128:129], off offset:48
	global_load_dwordx4 v[150:153], v[128:129], off offset:32
	global_load_dwordx4 v[178:181], v[128:129], off offset:16
	global_load_dwordx4 v[182:185], v[128:129], off
	s_branch .LBB0_3491

.LBB0_3495:
	s_mov_b32 s57, s56
	v_pk_mul_f32 v[72:73], s[56:57], v[94:95]
	s_and_b64 vcc, exec, s[4:5]
	v_cvt_pk_bf16_f32 v86, v72, v73
	v_pk_mul_f32 v[72:73], s[56:57], v[90:91]
	s_nop 0
	v_cvt_pk_bf16_f32 v87, v72, v73
	v_pk_mul_f32 v[72:73], s[56:57], v[88:89]
	s_nop 0
	v_cvt_pk_bf16_f32 v88, v72, v73
	v_pk_mul_f32 v[72:73], s[56:57], v[84:85]
	s_nop 0
	v_cvt_pk_bf16_f32 v89, v72, v73
	v_pk_mul_f32 v[72:73], s[56:57], v[98:99]
	s_nop 0
	v_cvt_pk_bf16_f32 v82, v72, v73
	v_pk_mul_f32 v[72:73], s[56:57], v[78:79]
	s_nop 0
	v_cvt_pk_bf16_f32 v83, v72, v73
	v_pk_mul_f32 v[72:73], s[56:57], v[76:77]
	s_nop 0
	v_cvt_pk_bf16_f32 v84, v72, v73
	v_pk_mul_f32 v[72:73], s[56:57], v[74:75]
	s_nop 0
	v_cvt_pk_bf16_f32 v85, v72, v73
	v_lshl_add_u64 v[72:73], v[80:81], 1, s[54:55]
	global_store_dwordx4 v[72:73], v[86:89], off
	v_lshl_add_u64 v[72:73], v[72:73], 0, s[92:93]
	global_store_dwordx4 v[72:73], v[82:85], off
	v_or_b32_e32 v72, 32, v18
	v_ashrrev_i32_e32 v73, 31, v72
	s_cbranch_vccnz .LBB0_3497
	v_lshlrev_b64 v[74:75], s64, v[72:73]
	v_lshl_add_u64 v[74:75], v[74:75], 3, v[68:69]
	v_mov_b32_e32 v94, v173
	v_mov_b32_e32 v95, v141
	s_waitcnt vmcnt(8)
	v_mov_b64_e32 v[96:97], v[154:155]
	v_mov_b64_e32 v[98:99], v[156:157]
	v_mov_b64_e32 v[84:85], v[158:159]
	v_mov_b64_e32 v[86:87], v[160:161]
	v_mov_b64_e32 v[80:81], v[186:187]
	v_mov_b64_e32 v[82:83], v[188:189]
	v_mov_b64_e32 v[76:77], v[190:191]
	v_mov_b64_e32 v[78:79], v[192:193]
	v_pk_mul_f32 v[94:95], v[94:95], v[98:99]
	s_nop 0
	v_mov_b32_e32 v103, v94
	v_mov_b32_e32 v105, v95
	v_mov_b32_e32 v75, v78
	v_mov_b32_e32 v78, v77
	v_mov_b32_e32 v74, v76
	v_pk_mul_f32 v[90:91], v[142:143], v[78:79]
	v_pk_mul_f32 v[76:77], v[174:175], v[78:79]
	v_mov_b32_e32 v79, v82
	v_mov_b32_e32 v82, v81
	v_mov_b32_e32 v78, v80
	v_pk_mul_f32 v[92:93], v[144:145], v[82:83]
	v_pk_mul_f32 v[80:81], v[176:177], v[82:83]
	v_mov_b32_e32 v83, v86
	v_mov_b32_e32 v86, v85
	v_mov_b32_e32 v82, v84
	v_pk_mul_f32 v[100:101], v[138:139], v[86:87]
	v_pk_fma_f32 v[94:95], v[176:177], v[78:79], v[92:93] neg_lo:[0,0,1] neg_hi:[0,0,1]
	v_pk_fma_f32 v[92:93], v[170:171], v[82:83], v[100:101] neg_lo:[0,0,1] neg_hi:[0,0,1]
	v_mov_b32_e32 v100, v141
	v_mov_b32_e32 v101, v173
	v_pk_mul_f32 v[98:99], v[100:101], v[98:99]
	v_pk_mul_f32 v[84:85], v[170:171], v[86:87]
	v_mul_f32_e32 v102, v172, v96
	v_mul_f32_e32 v104, v140, v97
	v_mul_f32_e32 v86, v140, v96
	v_mul_f32_e32 v88, v172, v97
	v_mov_b32_e32 v87, v98
	v_mov_b32_e32 v89, v99
	v_pk_fma_f32 v[96:97], v[174:175], v[74:75], v[90:91] neg_lo:[0,0,1] neg_hi:[0,0,1]
	v_pk_add_f32 v[90:91], v[102:103], v[104:105] neg_lo:[0,1] neg_hi:[0,1]
	v_pk_fma_f32 v[98:99], v[142:143], v[74:75], v[76:77]
	v_pk_fma_f32 v[78:79], v[144:145], v[78:79], v[80:81]
	v_pk_fma_f32 v[76:77], v[138:139], v[82:83], v[84:85]
	v_pk_add_f32 v[74:75], v[86:87], v[88:89]
	s_and_b64 vcc, exec, s[6:7]
	s_mov_b64 s[60:61], -1
	v_add_u32_e32 v128, 0x80, v18
	v_ashrrev_i32_e32 v129, 31, v128
	v_lshlrev_b64 v[128:129], s64, v[128:129]
	v_lshl_add_u64 v[128:129], v[128:129], 3, v[68:69]
	global_load_dwordx4 v[106:109], v[128:129], off offset:48
	global_load_dwordx4 v[110:113], v[128:129], off offset:32
	global_load_dwordx4 v[114:117], v[128:129], off offset:16
	global_load_dwordx4 v[118:121], v[128:129], off
	s_cbranch_vccz .LBB0_3498
	s_branch .LBB0_3499

.LBB0_3501:
	v_pk_mul_f32 v[72:73], s[56:57], v[96:97]
	s_and_b64 vcc, exec, s[4:5]
	v_cvt_pk_bf16_f32 v82, v72, v73
	v_pk_mul_f32 v[72:73], s[56:57], v[94:95]
	s_nop 0
	v_cvt_pk_bf16_f32 v83, v72, v73
	v_pk_mul_f32 v[72:73], s[56:57], v[92:93]
	s_nop 0
	v_cvt_pk_bf16_f32 v84, v72, v73
	v_pk_mul_f32 v[72:73], s[56:57], v[90:91]
	s_nop 0
	v_cvt_pk_bf16_f32 v85, v72, v73
	v_pk_mul_f32 v[72:73], s[56:57], v[98:99]
	s_nop 0
	v_cvt_pk_bf16_f32 v86, v72, v73
	v_pk_mul_f32 v[72:73], s[56:57], v[78:79]
	s_nop 0
	v_cvt_pk_bf16_f32 v87, v72, v73
	v_pk_mul_f32 v[72:73], s[56:57], v[76:77]
	s_nop 0
	v_cvt_pk_bf16_f32 v88, v72, v73
	v_pk_mul_f32 v[72:73], s[56:57], v[74:75]
	s_nop 0
	v_cvt_pk_bf16_f32 v89, v72, v73
	v_lshl_add_u64 v[72:73], v[80:81], 1, s[54:55]
	global_store_dwordx4 v[72:73], v[82:85], off
	v_lshl_add_u64 v[72:73], v[72:73], 0, s[92:93]
	global_store_dwordx4 v[72:73], v[86:89], off
	v_or_b32_e32 v72, 48, v18
	v_ashrrev_i32_e32 v73, 31, v72
	s_cbranch_vccnz .LBB0_3503
	v_lshlrev_b64 v[74:75], s64, v[72:73]
	v_lshl_add_u64 v[74:75], v[74:75], 3, v[68:69]
	v_mov_b32_e32 v94, v165
	v_mov_b32_e32 v95, v133
	s_waitcnt vmcnt(8)
	v_mov_b64_e32 v[96:97], v[146:147]
	v_mov_b64_e32 v[98:99], v[148:149]
	v_mov_b64_e32 v[84:85], v[150:151]
	v_mov_b64_e32 v[86:87], v[152:153]
	v_mov_b64_e32 v[80:81], v[178:179]
	v_mov_b64_e32 v[82:83], v[180:181]
	v_mov_b64_e32 v[76:77], v[182:183]
	v_mov_b64_e32 v[78:79], v[184:185]
	v_pk_mul_f32 v[94:95], v[94:95], v[98:99]
	s_nop 0
	v_mov_b32_e32 v103, v94
	v_mov_b32_e32 v105, v95
	v_mov_b32_e32 v75, v78
	v_mov_b32_e32 v78, v77
	v_mov_b32_e32 v74, v76
	v_pk_mul_f32 v[90:91], v[134:135], v[78:79]
	v_pk_mul_f32 v[76:77], v[166:167], v[78:79]
	v_mov_b32_e32 v79, v82
	v_mov_b32_e32 v82, v81
	v_mov_b32_e32 v78, v80
	v_pk_mul_f32 v[92:93], v[136:137], v[82:83]
	v_pk_mul_f32 v[80:81], v[168:169], v[82:83]
	v_mov_b32_e32 v83, v86
	v_mov_b32_e32 v86, v85
	v_mov_b32_e32 v82, v84
	v_pk_mul_f32 v[100:101], v[130:131], v[86:87]
	v_pk_fma_f32 v[94:95], v[168:169], v[78:79], v[92:93] neg_lo:[0,0,1] neg_hi:[0,0,1]
	v_pk_fma_f32 v[92:93], v[162:163], v[82:83], v[100:101] neg_lo:[0,0,1] neg_hi:[0,0,1]
	v_mov_b32_e32 v100, v133
	v_mov_b32_e32 v101, v165
	v_pk_mul_f32 v[98:99], v[100:101], v[98:99]
	v_pk_mul_f32 v[84:85], v[162:163], v[86:87]
	v_mul_f32_e32 v102, v164, v96
	v_mul_f32_e32 v104, v132, v97
	v_mul_f32_e32 v86, v132, v96
	v_mul_f32_e32 v88, v164, v97
	v_mov_b32_e32 v87, v98
	v_mov_b32_e32 v89, v99
	v_pk_fma_f32 v[96:97], v[166:167], v[74:75], v[90:91] neg_lo:[0,0,1] neg_hi:[0,0,1]
	v_pk_add_f32 v[90:91], v[102:103], v[104:105] neg_lo:[0,1] neg_hi:[0,1]
	v_pk_fma_f32 v[98:99], v[134:135], v[74:75], v[76:77]
	v_pk_fma_f32 v[78:79], v[136:137], v[78:79], v[80:81]
	v_pk_fma_f32 v[76:77], v[130:131], v[82:83], v[84:85]
	v_pk_add_f32 v[74:75], v[86:87], v[88:89]
	s_and_b64 vcc, exec, s[6:7]
	s_mov_b64 s[60:61], -1
	v_add_u32_e32 v128, 0x90, v18
	v_ashrrev_i32_e32 v129, 31, v128
	v_lshlrev_b64 v[128:129], s64, v[128:129]
	v_lshl_add_u64 v[128:129], v[128:129], 3, v[68:69]
	global_load_dwordx4 v[154:157], v[128:129], off offset:48
	global_load_dwordx4 v[158:161], v[128:129], off offset:32
	global_load_dwordx4 v[186:189], v[128:129], off offset:16
	global_load_dwordx4 v[190:193], v[128:129], off
	s_cbranch_vccz .LBB0_3504
	s_branch .LBB0_3505

.LBB0_3507:
	v_pk_mul_f32 v[72:73], s[56:57], v[96:97]
	s_and_b64 vcc, exec, s[4:5]
	v_cvt_pk_bf16_f32 v82, v72, v73
	v_pk_mul_f32 v[72:73], s[56:57], v[94:95]
	s_nop 0
	v_cvt_pk_bf16_f32 v83, v72, v73
	v_pk_mul_f32 v[72:73], s[56:57], v[92:93]
	s_nop 0
	v_cvt_pk_bf16_f32 v84, v72, v73
	v_pk_mul_f32 v[72:73], s[56:57], v[90:91]
	s_nop 0
	v_cvt_pk_bf16_f32 v85, v72, v73
	v_pk_mul_f32 v[72:73], s[56:57], v[98:99]
	s_nop 0
	v_cvt_pk_bf16_f32 v86, v72, v73
	v_pk_mul_f32 v[72:73], s[56:57], v[78:79]
	s_nop 0
	v_cvt_pk_bf16_f32 v87, v72, v73
	v_pk_mul_f32 v[72:73], s[56:57], v[76:77]
	s_nop 0
	v_cvt_pk_bf16_f32 v88, v72, v73
	v_pk_mul_f32 v[72:73], s[56:57], v[74:75]
	s_nop 0
	v_cvt_pk_bf16_f32 v89, v72, v73
	v_lshl_add_u64 v[72:73], v[80:81], 1, s[54:55]
	global_store_dwordx4 v[72:73], v[82:85], off
	v_lshl_add_u64 v[72:73], v[72:73], 0, s[92:93]
	global_store_dwordx4 v[72:73], v[86:89], off
	v_add_u32_e32 v72, 0x80, v18
	v_ashrrev_i32_e32 v73, 31, v72
	s_cbranch_vccnz .LBB0_3509
	v_lshlrev_b64 v[74:75], s64, v[72:73]
	v_lshl_add_u64 v[74:75], v[74:75], 3, v[68:69]
	v_mov_b32_e32 v94, v57
	v_mov_b32_e32 v95, v53
	s_waitcnt vmcnt(8)
	v_mov_b64_e32 v[96:97], v[106:107]
	v_mov_b64_e32 v[98:99], v[108:109]
	v_mov_b64_e32 v[84:85], v[110:111]
	v_mov_b64_e32 v[86:87], v[112:113]
	v_mov_b64_e32 v[80:81], v[114:115]
	v_mov_b64_e32 v[82:83], v[116:117]
	v_mov_b64_e32 v[76:77], v[118:119]
	v_mov_b64_e32 v[78:79], v[120:121]
	v_pk_mul_f32 v[94:95], v[94:95], v[98:99]
	v_mul_f32_e32 v100, v56, v96
	v_mul_f32_e32 v102, v52, v97
	v_mov_b32_e32 v75, v78
	v_mov_b32_e32 v78, v77
	v_mov_b32_e32 v74, v76
	v_pk_mul_f32 v[88:89], v[62:63], v[78:79]
	v_pk_mul_f32 v[76:77], v[126:127], v[78:79]
	v_mov_b32_e32 v79, v82
	v_mov_b32_e32 v82, v81
	v_mov_b32_e32 v78, v80
	v_pk_mul_f32 v[90:91], v[54:55], v[82:83]
	v_pk_mul_f32 v[80:81], v[60:61], v[82:83]
	v_mov_b32_e32 v83, v86
	v_mov_b32_e32 v86, v85
	v_mov_b32_e32 v82, v84
	v_pk_mul_f32 v[84:85], v[58:59], v[86:87]
	v_mov_b32_e32 v101, v94
	v_mov_b32_e32 v103, v95
	v_pk_fma_f32 v[94:95], v[126:127], v[74:75], v[88:89] neg_lo:[0,0,1] neg_hi:[0,0,1]
	v_pk_fma_f32 v[88:89], v[64:65], v[82:83], v[84:85] neg_lo:[0,0,1] neg_hi:[0,0,1]
	v_pk_add_f32 v[84:85], v[100:101], v[102:103] neg_lo:[0,1] neg_hi:[0,1]
	v_mov_b32_e32 v100, v53
	v_mov_b32_e32 v101, v57
	v_pk_mul_f32 v[98:99], v[100:101], v[98:99]
	v_pk_mul_f32 v[86:87], v[64:65], v[86:87]
	v_mul_f32_e32 v92, v52, v96
	v_mul_f32_e32 v96, v56, v97
	v_mov_b32_e32 v93, v98
	v_mov_b32_e32 v97, v99
	v_pk_fma_f32 v[90:91], v[60:61], v[78:79], v[90:91] neg_lo:[0,0,1] neg_hi:[0,0,1]
	v_pk_fma_f32 v[98:99], v[62:63], v[74:75], v[76:77]
	v_pk_fma_f32 v[78:79], v[54:55], v[78:79], v[80:81]
	v_pk_fma_f32 v[76:77], v[58:59], v[82:83], v[86:87]
	v_pk_add_f32 v[74:75], v[92:93], v[96:97]
	s_and_b64 vcc, exec, s[6:7]
	s_mov_b64 s[60:61], -1
	v_add_u32_e32 v128, 0xa0, v18
	v_ashrrev_i32_e32 v129, 31, v128
	v_lshlrev_b64 v[128:129], s64, v[128:129]
	v_lshl_add_u64 v[128:129], v[128:129], 3, v[68:69]
	global_load_dwordx4 v[146:149], v[128:129], off offset:48
	global_load_dwordx4 v[150:153], v[128:129], off offset:32
	global_load_dwordx4 v[178:181], v[128:129], off offset:16
	global_load_dwordx4 v[182:185], v[128:129], off
	s_cbranch_vccz .LBB0_3510
	s_branch .LBB0_3511

.LBB0_3513:
	v_pk_mul_f32 v[72:73], s[56:57], v[94:95]
	s_and_b64 vcc, exec, s[4:5]
	v_cvt_pk_bf16_f32 v86, v72, v73
	v_pk_mul_f32 v[72:73], s[56:57], v[90:91]
	s_mov_b32 s65, 0x800000
	v_cvt_pk_bf16_f32 v87, v72, v73
	v_pk_mul_f32 v[72:73], s[56:57], v[88:89]
	s_nop 0
	v_cvt_pk_bf16_f32 v88, v72, v73
	v_pk_mul_f32 v[72:73], s[56:57], v[84:85]
	s_nop 0
	v_cvt_pk_bf16_f32 v89, v72, v73
	v_pk_mul_f32 v[72:73], s[56:57], v[98:99]
	s_nop 0
	v_cvt_pk_bf16_f32 v82, v72, v73
	v_pk_mul_f32 v[72:73], s[56:57], v[78:79]
	s_nop 0
	v_cvt_pk_bf16_f32 v83, v72, v73
	v_pk_mul_f32 v[72:73], s[56:57], v[76:77]
	s_nop 0
	v_cvt_pk_bf16_f32 v84, v72, v73
	v_pk_mul_f32 v[72:73], s[56:57], v[74:75]
	s_nop 0
	v_cvt_pk_bf16_f32 v85, v72, v73
	v_lshl_add_u64 v[72:73], v[80:81], 1, s[54:55]
	global_store_dwordx4 v[72:73], v[86:89], off
	v_lshl_add_u64 v[72:73], v[72:73], 0, s[92:93]
	global_store_dwordx4 v[72:73], v[82:85], off
	v_add_u32_e32 v72, 0x90, v18
	v_ashrrev_i32_e32 v73, 31, v72
	s_cbranch_vccnz .LBB0_3515
	v_lshlrev_b64 v[74:75], s64, v[72:73]
	v_lshl_add_u64 v[74:75], v[74:75], 3, v[68:69]
	v_mov_b32_e32 v94, v41
	v_mov_b32_e32 v95, v37
	s_waitcnt vmcnt(8)
	v_mov_b64_e32 v[96:97], v[154:155]
	v_mov_b64_e32 v[98:99], v[156:157]
	v_mov_b64_e32 v[84:85], v[158:159]
	v_mov_b64_e32 v[86:87], v[160:161]
	v_mov_b64_e32 v[80:81], v[186:187]
	v_mov_b64_e32 v[82:83], v[188:189]
	v_mov_b64_e32 v[76:77], v[190:191]
	v_mov_b64_e32 v[78:79], v[192:193]
	v_pk_mul_f32 v[94:95], v[94:95], v[98:99]
	s_nop 0
	v_mov_b32_e32 v103, v94
	v_mov_b32_e32 v105, v95
	v_mov_b32_e32 v75, v78
	v_mov_b32_e32 v78, v77
	v_mov_b32_e32 v74, v76
	v_pk_mul_f32 v[90:91], v[46:47], v[78:79]
	v_pk_mul_f32 v[76:77], v[50:51], v[78:79]
	v_mov_b32_e32 v79, v82
	v_mov_b32_e32 v82, v81
	v_mov_b32_e32 v78, v80
	v_pk_mul_f32 v[92:93], v[38:39], v[82:83]
	v_pk_mul_f32 v[80:81], v[44:45], v[82:83]
	v_mov_b32_e32 v83, v86
	v_mov_b32_e32 v86, v85
	v_mov_b32_e32 v82, v84
	v_pk_mul_f32 v[100:101], v[42:43], v[86:87]
	v_pk_fma_f32 v[94:95], v[44:45], v[78:79], v[92:93] neg_lo:[0,0,1] neg_hi:[0,0,1]
	v_pk_fma_f32 v[92:93], v[48:49], v[82:83], v[100:101] neg_lo:[0,0,1] neg_hi:[0,0,1]
	v_mov_b32_e32 v100, v37
	v_mov_b32_e32 v101, v41
	v_pk_mul_f32 v[98:99], v[100:101], v[98:99]
	v_pk_mul_f32 v[84:85], v[48:49], v[86:87]
	v_mul_f32_e32 v102, v40, v96
	v_mul_f32_e32 v104, v36, v97
	v_mul_f32_e32 v86, v36, v96
	v_mul_f32_e32 v88, v40, v97
	v_mov_b32_e32 v87, v98
	v_mov_b32_e32 v89, v99
	v_pk_fma_f32 v[96:97], v[50:51], v[74:75], v[90:91] neg_lo:[0,0,1] neg_hi:[0,0,1]
	v_pk_add_f32 v[90:91], v[102:103], v[104:105] neg_lo:[0,1] neg_hi:[0,1]
	v_pk_fma_f32 v[98:99], v[46:47], v[74:75], v[76:77]
	v_pk_fma_f32 v[78:79], v[38:39], v[78:79], v[80:81]
	v_pk_fma_f32 v[76:77], v[42:43], v[82:83], v[84:85]
	v_pk_add_f32 v[74:75], v[86:87], v[88:89]
	s_and_b64 vcc, exec, s[6:7]
	s_mov_b64 s[60:61], -1
	v_add_u32_e32 v128, 0xb0, v18
	v_ashrrev_i32_e32 v129, 31, v128
	v_lshlrev_b64 v[128:129], s64, v[128:129]
	v_lshl_add_u64 v[128:129], v[128:129], 3, v[68:69]
	global_load_dwordx4 v[106:109], v[128:129], off offset:48
	global_load_dwordx4 v[110:113], v[128:129], off offset:32
	global_load_dwordx4 v[114:117], v[128:129], off offset:16
	global_load_dwordx4 v[118:121], v[128:129], off
	s_cbranch_vccz .LBB0_3516
	s_branch .LBB0_3517

.LBB0_3519:
	v_pk_mul_f32 v[72:73], s[56:57], v[96:97]
	s_and_b64 vcc, exec, s[4:5]
	v_cvt_pk_bf16_f32 v82, v72, v73
	v_pk_mul_f32 v[72:73], s[56:57], v[94:95]
	s_nop 0
	v_cvt_pk_bf16_f32 v83, v72, v73
	v_pk_mul_f32 v[72:73], s[56:57], v[92:93]
	s_nop 0
	v_cvt_pk_bf16_f32 v84, v72, v73
	v_pk_mul_f32 v[72:73], s[56:57], v[90:91]
	s_nop 0
	v_cvt_pk_bf16_f32 v85, v72, v73
	v_pk_mul_f32 v[72:73], s[56:57], v[98:99]
	s_nop 0
	v_cvt_pk_bf16_f32 v86, v72, v73
	v_pk_mul_f32 v[72:73], s[56:57], v[78:79]
	s_nop 0
	v_cvt_pk_bf16_f32 v87, v72, v73
	v_pk_mul_f32 v[72:73], s[56:57], v[76:77]
	s_nop 0
	v_cvt_pk_bf16_f32 v88, v72, v73
	v_pk_mul_f32 v[72:73], s[56:57], v[74:75]
	s_nop 0
	v_cvt_pk_bf16_f32 v89, v72, v73
	v_lshl_add_u64 v[72:73], v[80:81], 1, s[54:55]
	global_store_dwordx4 v[72:73], v[82:85], off
	v_lshl_add_u64 v[72:73], v[72:73], 0, s[92:93]
	global_store_dwordx4 v[72:73], v[86:89], off
	v_add_u32_e32 v72, 0xa0, v18
	v_ashrrev_i32_e32 v73, 31, v72
	s_cbranch_vccnz .LBB0_3521
	v_lshlrev_b64 v[74:75], s64, v[72:73]
	v_lshl_add_u64 v[74:75], v[74:75], 3, v[68:69]
	v_mov_b32_e32 v94, v25
	v_mov_b32_e32 v95, v21
	s_waitcnt vmcnt(8)
	v_mov_b64_e32 v[96:97], v[146:147]
	v_mov_b64_e32 v[98:99], v[148:149]
	v_mov_b64_e32 v[84:85], v[150:151]
	v_mov_b64_e32 v[86:87], v[152:153]
	v_mov_b64_e32 v[80:81], v[178:179]
	v_mov_b64_e32 v[82:83], v[180:181]
	v_mov_b64_e32 v[76:77], v[182:183]
	v_mov_b64_e32 v[78:79], v[184:185]
	v_pk_mul_f32 v[94:95], v[94:95], v[98:99]
	s_nop 0
	v_mov_b32_e32 v103, v94
	v_mov_b32_e32 v105, v95
	v_mov_b32_e32 v75, v78
	v_mov_b32_e32 v78, v77
	v_mov_b32_e32 v74, v76
	v_pk_mul_f32 v[90:91], v[30:31], v[78:79]
	v_pk_mul_f32 v[76:77], v[34:35], v[78:79]
	v_mov_b32_e32 v79, v82
	v_mov_b32_e32 v82, v81
	v_mov_b32_e32 v78, v80
	v_pk_mul_f32 v[92:93], v[22:23], v[82:83]
	v_pk_mul_f32 v[80:81], v[28:29], v[82:83]
	v_mov_b32_e32 v83, v86
	v_mov_b32_e32 v86, v85
	v_mov_b32_e32 v82, v84
	v_pk_mul_f32 v[100:101], v[26:27], v[86:87]
	v_pk_fma_f32 v[94:95], v[28:29], v[78:79], v[92:93] neg_lo:[0,0,1] neg_hi:[0,0,1]
	v_pk_fma_f32 v[92:93], v[32:33], v[82:83], v[100:101] neg_lo:[0,0,1] neg_hi:[0,0,1]
	v_mov_b32_e32 v100, v21
	v_mov_b32_e32 v101, v25
	v_pk_mul_f32 v[98:99], v[100:101], v[98:99]
	v_pk_mul_f32 v[84:85], v[32:33], v[86:87]
	v_mul_f32_e32 v102, v24, v96
	v_mul_f32_e32 v104, v20, v97
	v_mul_f32_e32 v86, v20, v96
	v_mul_f32_e32 v88, v24, v97
	v_mov_b32_e32 v87, v98
	v_mov_b32_e32 v89, v99
	v_pk_fma_f32 v[96:97], v[34:35], v[74:75], v[90:91] neg_lo:[0,0,1] neg_hi:[0,0,1]
	v_pk_add_f32 v[90:91], v[102:103], v[104:105] neg_lo:[0,1] neg_hi:[0,1]
	v_pk_fma_f32 v[98:99], v[30:31], v[74:75], v[76:77]
	v_pk_fma_f32 v[78:79], v[22:23], v[78:79], v[80:81]
	v_pk_fma_f32 v[76:77], v[26:27], v[82:83], v[84:85]
	v_pk_add_f32 v[74:75], v[86:87], v[88:89]
	s_and_b64 vcc, exec, s[6:7]
	s_mov_b64 s[60:61], -1
	s_cbranch_vccz .LBB0_3522
	s_branch .LBB0_3523

.LBB0_3525:
	v_pk_mul_f32 v[72:73], s[56:57], v[96:97]
	s_and_b64 vcc, exec, s[4:5]
	v_cvt_pk_bf16_f32 v82, v72, v73
	v_pk_mul_f32 v[72:73], s[56:57], v[94:95]
	s_mov_b64 s[60:61], 0x400
	v_cvt_pk_bf16_f32 v83, v72, v73
	v_pk_mul_f32 v[72:73], s[56:57], v[92:93]
	s_nop 0
	v_cvt_pk_bf16_f32 v84, v72, v73
	v_pk_mul_f32 v[72:73], s[56:57], v[90:91]
	s_nop 0
	v_cvt_pk_bf16_f32 v85, v72, v73
	v_pk_mul_f32 v[72:73], s[56:57], v[98:99]
	s_nop 0
	v_cvt_pk_bf16_f32 v86, v72, v73
	v_pk_mul_f32 v[72:73], s[56:57], v[78:79]
	s_nop 0
	v_cvt_pk_bf16_f32 v87, v72, v73
	v_pk_mul_f32 v[72:73], s[56:57], v[76:77]
	s_nop 0
	v_cvt_pk_bf16_f32 v88, v72, v73
	v_pk_mul_f32 v[72:73], s[56:57], v[74:75]
	s_nop 0
	v_cvt_pk_bf16_f32 v89, v72, v73
	v_lshl_add_u64 v[72:73], v[80:81], 1, s[54:55]
	global_store_dwordx4 v[72:73], v[82:85], off
	v_lshl_add_u64 v[72:73], v[72:73], 0, s[92:93]
	global_store_dwordx4 v[72:73], v[86:89], off
	v_add_u32_e32 v72, 0xb0, v18
	v_ashrrev_i32_e32 v73, 31, v72
	s_cbranch_vccnz .LBB0_3527
	v_lshlrev_b64 v[74:75], s64, v[72:73]
	v_lshl_add_u64 v[68:69], v[74:75], 3, v[68:69]
	s_waitcnt vmcnt(4)
	v_mov_b64_e32 v[94:95], v[106:107]
	v_mov_b64_e32 v[96:97], v[108:109]
	v_mov_b64_e32 v[82:83], v[110:111]
	v_mov_b64_e32 v[84:85], v[112:113]
	v_mov_b64_e32 v[78:79], v[114:115]
	v_mov_b64_e32 v[80:81], v[116:117]
	v_mov_b64_e32 v[74:75], v[118:119]
	v_mov_b64_e32 v[76:77], v[120:121]
	v_mul_f32_e32 v100, v2, v95
	v_mul_f32_e32 v86, v2, v94
	v_mul_f32_e32 v90, v6, v95
	v_mov_b32_e32 v69, v76
	v_mov_b32_e32 v76, v75
	v_mov_b32_e32 v68, v74
	v_pk_mul_f32 v[88:89], v[12:13], v[76:77]
	v_pk_mul_f32 v[74:75], v[16:17], v[76:77]
	v_mov_b32_e32 v77, v80
	v_mov_b32_e32 v80, v79
	v_mov_b32_e32 v76, v78
	v_pk_mul_f32 v[92:93], v[4:5], v[80:81]
	v_pk_mul_f32 v[78:79], v[10:11], v[80:81]
	v_mov_b32_e32 v81, v84
	v_mov_b32_e32 v84, v83
	v_mov_b32_e32 v80, v82
	v_pk_mul_f32 v[98:99], v[8:9], v[84:85]
	v_pk_mul_f32 v[82:83], v[14:15], v[84:85]
	v_mul_f32_e32 v84, v6, v94
	v_mov_b32_e32 v94, v7
	v_mov_b32_e32 v95, v3
	v_pk_mul_f32 v[94:95], v[94:95], v[96:97]
	v_pk_fma_f32 v[92:93], v[10:11], v[76:77], v[92:93] neg_lo:[0,0,1] neg_hi:[0,0,1]
	v_mov_b32_e32 v85, v94
	v_mov_b32_e32 v101, v95
	v_pk_fma_f32 v[94:95], v[16:17], v[68:69], v[88:89] neg_lo:[0,0,1] neg_hi:[0,0,1]
	v_pk_fma_f32 v[88:89], v[14:15], v[80:81], v[98:99] neg_lo:[0,0,1] neg_hi:[0,0,1]
	v_mov_b32_e32 v98, v3
	v_mov_b32_e32 v99, v7
	v_pk_mul_f32 v[96:97], v[98:99], v[96:97]
	v_pk_add_f32 v[84:85], v[84:85], v[100:101] neg_lo:[0,1] neg_hi:[0,1]
	v_mov_b32_e32 v87, v96
	v_mov_b32_e32 v91, v97
	v_pk_fma_f32 v[96:97], v[12:13], v[68:69], v[74:75]
	v_pk_fma_f32 v[76:77], v[4:5], v[76:77], v[78:79]
	v_pk_fma_f32 v[74:75], v[8:9], v[80:81], v[82:83]
	v_pk_add_f32 v[68:69], v[86:87], v[90:91]
	s_movk_i32 s64, 0x1800
	s_and_b64 vcc, exec, s[6:7]
	s_mov_b64 s[4:5], -1
	s_cbranch_vccnz .LBB0_3529
	s_branch .LBB0_3528
